# stack12 = stack11 with both K loops as four 8-MFMA blocks per k-step (fragments 0-3 re-requested in block 2, 4-7 in block 4): loads spread over the whole k-step
# baseline (speedup 1.0000x reference)
; #define LOADB(dst, ks_) do { const unsigned char* ub_ = wb + (size_t)((ks_) * 144) * 1024; \
;         _Pragma("unroll") for (int j_ = 0; j_ < 8; ++j_) dst[j_] = *(const bf16x8*)(ub_ + j_ * 1024 + voff); } while (0)
; #define LOADA(fd, ks_) do { _Pragma("unroll") for (int mi_ = 0; mi_ < 4; ++mi_) fd[mi_] = AFRAG(mi_, ks_); } while (0)
; #define MMA(src, fs, ksn_) do { _Pragma("unroll") for (int mi_ = 0; mi_ < 4; ++mi_) { \
;         _Pragma("unroll") for (int j_ = 0; j_ < 8; ++j_) acc[j_][mi_] = __builtin_amdgcn_mfma_f32_16x16x32_bf16(src[j_], fs[mi_], acc[j_][mi_], 0, 0, 0); \
;         fs[mi_] = AFRAG(mi_, (ksn_) < 32 ? (ksn_) : 31); } } while (0)
; #define LOADB(dst, ks_) do { const unsigned char* ub_ = wb + (size_t)((ks_) * 64) * 1024; \
;         _Pragma("unroll") for (int j_ = 0; j_ < 8; ++j_) dst[j_] = *(const bf16x8*)(ub_ + j_ * 1024 + voff); } while (0)
; #define LOADA(fd, ks_) do { _Pragma("unroll") for (int mi_ = 0; mi_ < 4; ++mi_) fd[mi_] = AFRAG(mi_, ks_); } while (0)
; #define MMA(src, fs, ksn_) do { _Pragma("unroll") for (int mi_ = 0; mi_ < 4; ++mi_) { \
;         _Pragma("unroll") for (int j_ = 0; j_ < 8; ++j_) acc[j_][mi_] = __builtin_amdgcn_mfma_f32_16x16x32_bf16(src[j_], fs[mi_], acc[j_][mi_], 0, 0, 0); \
;         fs[mi_] = AFRAG(mi_, (ksn_) < 32 ? (ksn_) : 31); } } while (0)
; DEVINL void phase2(const Params& P, unsigned char* smem, XPre& X, const bool have_pre) {
;     ...
;                 bf16x8 fa[4];
;                 LOADB(b0, 0); LOADA(fa, 0);
; #pragma unroll 1
;                 for (int ks = 0; ks < 32; ks += 2) {
;                     LOADB(b1, ks + 1);
;                     __builtin_amdgcn_sched_barrier(0);
;                     MMA(b0, fa, ks + 1);
;                     __builtin_amdgcn_sched_barrier(0);
;                     LOADB(b0, ks + 2 < 32 ? ks + 2 : 31);
;                     __builtin_amdgcn_sched_barrier(0);
;                     MMA(b1, fa, ks + 2);
;                     __builtin_amdgcn_sched_barrier(0);
;                 }
.LBB0_206:
	s_add_i32 s1, s0, 2
	s_mul_i32 s18, s1, 0x24000
	s_add_i32 s18, s18, 0x1000
	v_xor_b32_e32 v252, v178, v181
	v_lshl_add_u32 v252, v252, 4, v212
	v_add_u32_e32 v253, 0x10000, v252
	v_lshl_add_u64 v[250:251], v[200:201], 0, s[18:19]
	s_waitcnt vmcnt(15) lgkmcnt(3)
	v_mfma_f32_16x16x32_bf16 v[126:129], v[130:133], v[174:177], v[126:129]
	s_waitcnt lgkmcnt(2)
	v_mfma_f32_16x16x32_bf16 v[110:113], v[130:133], v[170:173], v[110:113]
	s_waitcnt vmcnt(14)
	v_mfma_f32_16x16x32_bf16 v[118:121], v[134:137], v[174:177], v[118:121]
	v_mfma_f32_16x16x32_bf16 v[102:105], v[134:137], v[170:173], v[102:105]
	s_waitcnt vmcnt(13)
	v_mfma_f32_16x16x32_bf16 v[114:117], v[138:141], v[174:177], v[114:117]
	v_mfma_f32_16x16x32_bf16 v[98:101], v[138:141], v[170:173], v[98:101]
	s_waitcnt vmcnt(12)
	v_mfma_f32_16x16x32_bf16 v[122:125], v[142:145], v[174:177], v[122:125]
	v_mfma_f32_16x16x32_bf16 v[106:109], v[142:145], v[170:173], v[106:109]
	s_waitcnt lgkmcnt(1)
	v_mfma_f32_16x16x32_bf16 v[94:97], v[130:133], v[166:169], v[94:97]
	s_waitcnt lgkmcnt(0)
	v_mfma_f32_16x16x32_bf16 v[78:81], v[130:133], v[162:165], v[78:81]
	global_load_dwordx4 v[130:133], v[250:251], off offset:-4096
	v_mfma_f32_16x16x32_bf16 v[90:93], v[134:137], v[166:169], v[90:93]
	v_mfma_f32_16x16x32_bf16 v[74:77], v[134:137], v[162:165], v[74:77]
	global_load_dwordx4 v[134:137], v[250:251], off offset:-3072
	v_mfma_f32_16x16x32_bf16 v[82:85], v[138:141], v[166:169], v[82:85]
	v_mfma_f32_16x16x32_bf16 v[66:69], v[138:141], v[162:165], v[66:69]
	global_load_dwordx4 v[138:141], v[250:251], off offset:-2048
	v_mfma_f32_16x16x32_bf16 v[86:89], v[142:145], v[166:169], v[86:89]
	v_mfma_f32_16x16x32_bf16 v[70:73], v[142:145], v[162:165], v[70:73]
	global_load_dwordx4 v[142:145], v[250:251], off offset:-1024
	s_waitcnt vmcnt(15)
	v_mfma_f32_16x16x32_bf16 v[62:65], v[158:161], v[174:177], v[62:65]
	v_mfma_f32_16x16x32_bf16 v[46:49], v[158:161], v[170:173], v[46:49]
	s_waitcnt vmcnt(14)
	v_mfma_f32_16x16x32_bf16 v[54:57], v[154:157], v[174:177], v[54:57]
	v_mfma_f32_16x16x32_bf16 v[38:41], v[154:157], v[170:173], v[38:41]
	s_waitcnt vmcnt(13)
	v_mfma_f32_16x16x32_bf16 v[50:53], v[150:153], v[174:177], v[50:53]
	v_mfma_f32_16x16x32_bf16 v[34:37], v[150:153], v[170:173], v[34:37]
	s_waitcnt vmcnt(12)
	v_mfma_f32_16x16x32_bf16 v[58:61], v[146:149], v[174:177], v[58:61]
	v_mfma_f32_16x16x32_bf16 v[42:45], v[146:149], v[170:173], v[42:45]
	v_mfma_f32_16x16x32_bf16 v[30:33], v[158:161], v[166:169], v[30:33]
	v_mfma_f32_16x16x32_bf16 v[14:17], v[158:161], v[162:165], v[14:17]
	global_load_dwordx4 v[158:161], v[250:251], off
	ds_read_b128 v[174:177], v252
	v_mfma_f32_16x16x32_bf16 v[22:25], v[154:157], v[166:169], v[22:25]
	v_mfma_f32_16x16x32_bf16 v[10:13], v[154:157], v[162:165], v[10:13]
	global_load_dwordx4 v[154:157], v[250:251], off offset:1024
	ds_read_b128 v[170:173], v252 offset:32768
	v_mfma_f32_16x16x32_bf16 v[18:21], v[150:153], v[166:169], v[18:21]
	v_mfma_f32_16x16x32_bf16 v[2:5], v[150:153], v[162:165], v[2:5]
	global_load_dwordx4 v[150:153], v[250:251], off offset:2048
	v_mfma_f32_16x16x32_bf16 v[26:29], v[146:149], v[166:169], v[26:29]
	v_mfma_f32_16x16x32_bf16 v[6:9], v[146:149], v[162:165], v[6:9]
	global_load_dwordx4 v[146:149], v[250:251], off offset:3072
	ds_read_b128 v[166:169], v253
	ds_read_b128 v[162:165], v253 offset:32768
	s_mov_b64 s[6:7], 0x48000
	v_lshl_add_u32 v252, s1, 2, v211
	v_lshl_add_u64 v[202:203], v[202:203], 0, s[6:7]
	v_xor_b32_e32 v252, v252, v181
	v_lshl_add_u32 v252, v252, 4, v212
	v_add_u32_e32 v253, 0x10000, v252
	s_waitcnt vmcnt(15) lgkmcnt(3)
	v_mfma_f32_16x16x32_bf16 v[126:129], v[218:221], v[174:177], v[126:129]
	s_waitcnt lgkmcnt(2)
	v_mfma_f32_16x16x32_bf16 v[110:113], v[218:221], v[170:173], v[110:113]
	s_waitcnt vmcnt(14)
	v_mfma_f32_16x16x32_bf16 v[118:121], v[222:225], v[174:177], v[118:121]
	v_mfma_f32_16x16x32_bf16 v[102:105], v[222:225], v[170:173], v[102:105]
	s_waitcnt vmcnt(13)
	v_mfma_f32_16x16x32_bf16 v[114:117], v[226:229], v[174:177], v[114:117]
	v_mfma_f32_16x16x32_bf16 v[98:101], v[226:229], v[170:173], v[98:101]
	s_waitcnt vmcnt(12)
	v_mfma_f32_16x16x32_bf16 v[122:125], v[230:233], v[174:177], v[122:125]
	v_mfma_f32_16x16x32_bf16 v[106:109], v[230:233], v[170:173], v[106:109]
	s_waitcnt lgkmcnt(1)
	v_mfma_f32_16x16x32_bf16 v[94:97], v[218:221], v[166:169], v[94:97]
	s_waitcnt lgkmcnt(0)
	v_mfma_f32_16x16x32_bf16 v[78:81], v[218:221], v[162:165], v[78:81]
	global_load_dwordx4 v[218:221], v[202:203], off offset:-4096
	v_mfma_f32_16x16x32_bf16 v[90:93], v[222:225], v[166:169], v[90:93]
	v_mfma_f32_16x16x32_bf16 v[74:77], v[222:225], v[162:165], v[74:77]
	global_load_dwordx4 v[222:225], v[202:203], off offset:-3072
	v_mfma_f32_16x16x32_bf16 v[82:85], v[226:229], v[166:169], v[82:85]
	v_mfma_f32_16x16x32_bf16 v[66:69], v[226:229], v[162:165], v[66:69]
	global_load_dwordx4 v[226:229], v[202:203], off offset:-2048
	v_mfma_f32_16x16x32_bf16 v[86:89], v[230:233], v[166:169], v[86:89]
	v_mfma_f32_16x16x32_bf16 v[70:73], v[230:233], v[162:165], v[70:73]
	global_load_dwordx4 v[230:233], v[202:203], off offset:-1024
	s_waitcnt vmcnt(15)
	v_mfma_f32_16x16x32_bf16 v[62:65], v[234:237], v[174:177], v[62:65]
	v_mfma_f32_16x16x32_bf16 v[46:49], v[234:237], v[170:173], v[46:49]
	s_waitcnt vmcnt(14)
	v_mfma_f32_16x16x32_bf16 v[54:57], v[238:241], v[174:177], v[54:57]
	v_mfma_f32_16x16x32_bf16 v[38:41], v[238:241], v[170:173], v[38:41]
	s_waitcnt vmcnt(13)
	v_mfma_f32_16x16x32_bf16 v[50:53], v[242:245], v[174:177], v[50:53]
	v_mfma_f32_16x16x32_bf16 v[34:37], v[242:245], v[170:173], v[34:37]
	s_waitcnt vmcnt(12)
	v_mfma_f32_16x16x32_bf16 v[58:61], v[246:249], v[174:177], v[58:61]
	v_mfma_f32_16x16x32_bf16 v[42:45], v[246:249], v[170:173], v[42:45]
	v_mfma_f32_16x16x32_bf16 v[30:33], v[234:237], v[166:169], v[30:33]
	v_mfma_f32_16x16x32_bf16 v[14:17], v[234:237], v[162:165], v[14:17]
	global_load_dwordx4 v[234:237], v[202:203], off
	ds_read_b128 v[174:177], v252
	v_mfma_f32_16x16x32_bf16 v[22:25], v[238:241], v[166:169], v[22:25]
	v_mfma_f32_16x16x32_bf16 v[10:13], v[238:241], v[162:165], v[10:13]
	global_load_dwordx4 v[238:241], v[202:203], off offset:1024
	ds_read_b128 v[170:173], v252 offset:32768
	v_mfma_f32_16x16x32_bf16 v[18:21], v[242:245], v[166:169], v[18:21]
	v_mfma_f32_16x16x32_bf16 v[2:5], v[242:245], v[162:165], v[2:5]
	global_load_dwordx4 v[242:245], v[202:203], off offset:2048
	v_mfma_f32_16x16x32_bf16 v[26:29], v[246:249], v[166:169], v[26:29]
	v_mfma_f32_16x16x32_bf16 v[6:9], v[246:249], v[162:165], v[6:9]
	global_load_dwordx4 v[246:249], v[202:203], off offset:3072
	ds_read_b128 v[166:169], v253
	ds_read_b128 v[162:165], v253 offset:32768
	v_add_u32_e32 v178, 8, v178
	s_mov_b32 s0, s1
	s_cmp_lt_u32 s0, 30
	s_cbranch_scc1 .LBB0_206
; #define LOADB(dst, ks_) do { const unsigned char* ub_ = wb + (size_t)((ks_) * 144) * 1024; \
;         _Pragma("unroll") for (int j_ = 0; j_ < 8; ++j_) dst[j_] = *(const bf16x8*)(ub_ + j_ * 1024 + voff); } while (0)
; #define LOADA(fd, ks_) do { _Pragma("unroll") for (int mi_ = 0; mi_ < 4; ++mi_) fd[mi_] = AFRAG(mi_, ks_); } while (0)
; #define MMA(src, fs, ksn_) do { _Pragma("unroll") for (int mi_ = 0; mi_ < 4; ++mi_) { \
;         _Pragma("unroll") for (int j_ = 0; j_ < 8; ++j_) acc[j_][mi_] = __builtin_amdgcn_mfma_f32_16x16x32_bf16(src[j_], fs[mi_], acc[j_][mi_], 0, 0, 0); \
;         fs[mi_] = AFRAG(mi_, (ksn_) < 32 ? (ksn_) : 31); } } while (0)
; #define LOADB(dst, ks_) do { const unsigned char* ub_ = wb + (size_t)((ks_) * 64) * 1024; \
;         _Pragma("unroll") for (int j_ = 0; j_ < 8; ++j_) dst[j_] = *(const bf16x8*)(ub_ + j_ * 1024 + voff); } while (0)
; #define LOADA(fd, ks_) do { _Pragma("unroll") for (int mi_ = 0; mi_ < 4; ++mi_) fd[mi_] = AFRAG(mi_, ks_); } while (0)
; #define MMA(src, fs, ksn_) do { _Pragma("unroll") for (int mi_ = 0; mi_ < 4; ++mi_) { \
;         _Pragma("unroll") for (int j_ = 0; j_ < 8; ++j_) acc[j_][mi_] = __builtin_amdgcn_mfma_f32_16x16x32_bf16(src[j_], fs[mi_], acc[j_][mi_], 0, 0, 0); \
;         fs[mi_] = AFRAG(mi_, (ksn_) < 32 ? (ksn_) : 31); } } while (0)
; DEVINL void phase2(const Params& P, unsigned char* smem, XPre& X, const bool have_pre) {
;     ...
;                 bf16x8 fa[4];
;                 LOADB(b0, 0); LOADA(fa, 0);
; #pragma unroll 1
;                 for (int ks = 0; ks < 32; ks += 2) {
;                     LOADB(b1, ks + 1);
;                     __builtin_amdgcn_sched_barrier(0);
;                     MMA(b0, fa, ks + 1);
;                     __builtin_amdgcn_sched_barrier(0);
;                     LOADB(b0, ks + 2 < 32 ? ks + 2 : 31);
;                     __builtin_amdgcn_sched_barrier(0);
;                     MMA(b1, fa, ks + 2);
;                     __builtin_amdgcn_sched_barrier(0);
;                 }
	v_xor_b32_e32 v252, v178, v181
	v_lshl_add_u32 v252, v252, 4, v212
	v_add_u32_e32 v253, 0x10000, v252
	s_waitcnt vmcnt(15) lgkmcnt(3)
	v_mfma_f32_16x16x32_bf16 v[126:129], v[130:133], v[174:177], v[126:129]
	s_waitcnt lgkmcnt(2)
	v_mfma_f32_16x16x32_bf16 v[110:113], v[130:133], v[170:173], v[110:113]
	s_waitcnt vmcnt(14)
	v_mfma_f32_16x16x32_bf16 v[118:121], v[134:137], v[174:177], v[118:121]
	v_mfma_f32_16x16x32_bf16 v[102:105], v[134:137], v[170:173], v[102:105]
	s_waitcnt vmcnt(13)
	v_mfma_f32_16x16x32_bf16 v[114:117], v[138:141], v[174:177], v[114:117]
	v_mfma_f32_16x16x32_bf16 v[98:101], v[138:141], v[170:173], v[98:101]
	s_waitcnt vmcnt(12)
	v_mfma_f32_16x16x32_bf16 v[122:125], v[142:145], v[174:177], v[122:125]
	v_mfma_f32_16x16x32_bf16 v[106:109], v[142:145], v[170:173], v[106:109]
	s_waitcnt lgkmcnt(1)
	v_mfma_f32_16x16x32_bf16 v[94:97], v[130:133], v[166:169], v[94:97]
	s_waitcnt lgkmcnt(0)
	v_mfma_f32_16x16x32_bf16 v[78:81], v[130:133], v[162:165], v[78:81]
	v_mfma_f32_16x16x32_bf16 v[90:93], v[134:137], v[166:169], v[90:93]
	v_mfma_f32_16x16x32_bf16 v[74:77], v[134:137], v[162:165], v[74:77]
	v_mfma_f32_16x16x32_bf16 v[82:85], v[138:141], v[166:169], v[82:85]
	v_mfma_f32_16x16x32_bf16 v[66:69], v[138:141], v[162:165], v[66:69]
	v_mfma_f32_16x16x32_bf16 v[86:89], v[142:145], v[166:169], v[86:89]
	v_mfma_f32_16x16x32_bf16 v[70:73], v[142:145], v[162:165], v[70:73]
	s_waitcnt vmcnt(11)
	v_mfma_f32_16x16x32_bf16 v[62:65], v[158:161], v[174:177], v[62:65]
	v_mfma_f32_16x16x32_bf16 v[46:49], v[158:161], v[170:173], v[46:49]
	s_waitcnt vmcnt(10)
	v_mfma_f32_16x16x32_bf16 v[54:57], v[154:157], v[174:177], v[54:57]
	v_mfma_f32_16x16x32_bf16 v[38:41], v[154:157], v[170:173], v[38:41]
	s_waitcnt vmcnt(9)
	v_mfma_f32_16x16x32_bf16 v[50:53], v[150:153], v[174:177], v[50:53]
	v_mfma_f32_16x16x32_bf16 v[34:37], v[150:153], v[170:173], v[34:37]
	s_waitcnt vmcnt(8)
	v_mfma_f32_16x16x32_bf16 v[58:61], v[146:149], v[174:177], v[58:61]
	v_mfma_f32_16x16x32_bf16 v[42:45], v[146:149], v[170:173], v[42:45]
	v_mfma_f32_16x16x32_bf16 v[30:33], v[158:161], v[166:169], v[30:33]
	v_mfma_f32_16x16x32_bf16 v[14:17], v[158:161], v[162:165], v[14:17]
	ds_read_b128 v[174:177], v252
	v_mfma_f32_16x16x32_bf16 v[22:25], v[154:157], v[166:169], v[22:25]
	v_mfma_f32_16x16x32_bf16 v[10:13], v[154:157], v[162:165], v[10:13]
	ds_read_b128 v[170:173], v252 offset:32768
	v_mfma_f32_16x16x32_bf16 v[18:21], v[150:153], v[166:169], v[18:21]
	v_mfma_f32_16x16x32_bf16 v[2:5], v[150:153], v[162:165], v[2:5]
	v_mfma_f32_16x16x32_bf16 v[26:29], v[146:149], v[166:169], v[26:29]
	v_mfma_f32_16x16x32_bf16 v[6:9], v[146:149], v[162:165], v[6:9]
	ds_read_b128 v[166:169], v253
	ds_read_b128 v[162:165], v253 offset:32768
	s_waitcnt vmcnt(7) lgkmcnt(3)
	v_mfma_f32_16x16x32_bf16 v[126:129], v[218:221], v[174:177], v[126:129]
	s_waitcnt lgkmcnt(2)
	v_mfma_f32_16x16x32_bf16 v[110:113], v[218:221], v[170:173], v[110:113]
	s_waitcnt vmcnt(6)
	v_mfma_f32_16x16x32_bf16 v[118:121], v[222:225], v[174:177], v[118:121]
	v_mfma_f32_16x16x32_bf16 v[102:105], v[222:225], v[170:173], v[102:105]
	s_waitcnt vmcnt(5)
	v_mfma_f32_16x16x32_bf16 v[114:117], v[226:229], v[174:177], v[114:117]
	v_mfma_f32_16x16x32_bf16 v[98:101], v[226:229], v[170:173], v[98:101]
	s_waitcnt vmcnt(4)
	v_mfma_f32_16x16x32_bf16 v[122:125], v[230:233], v[174:177], v[122:125]
	v_mfma_f32_16x16x32_bf16 v[106:109], v[230:233], v[170:173], v[106:109]
	s_waitcnt lgkmcnt(1)
	v_mfma_f32_16x16x32_bf16 v[94:97], v[218:221], v[166:169], v[94:97]
	s_waitcnt lgkmcnt(0)
	v_mfma_f32_16x16x32_bf16 v[78:81], v[218:221], v[162:165], v[78:81]
	v_mfma_f32_16x16x32_bf16 v[90:93], v[222:225], v[166:169], v[90:93]
	v_mfma_f32_16x16x32_bf16 v[74:77], v[222:225], v[162:165], v[74:77]
	v_mfma_f32_16x16x32_bf16 v[82:85], v[226:229], v[166:169], v[82:85]
	v_mfma_f32_16x16x32_bf16 v[66:69], v[226:229], v[162:165], v[66:69]
	v_mfma_f32_16x16x32_bf16 v[86:89], v[230:233], v[166:169], v[86:89]
	v_mfma_f32_16x16x32_bf16 v[70:73], v[230:233], v[162:165], v[70:73]
	s_waitcnt vmcnt(3)
	v_mfma_f32_16x16x32_bf16 v[62:65], v[234:237], v[174:177], v[62:65]
	v_mfma_f32_16x16x32_bf16 v[46:49], v[234:237], v[170:173], v[46:49]
	s_waitcnt vmcnt(2)
	v_mfma_f32_16x16x32_bf16 v[54:57], v[238:241], v[174:177], v[54:57]
	v_mfma_f32_16x16x32_bf16 v[38:41], v[238:241], v[170:173], v[38:41]
	s_waitcnt vmcnt(1)
	v_mfma_f32_16x16x32_bf16 v[50:53], v[242:245], v[174:177], v[50:53]
	v_mfma_f32_16x16x32_bf16 v[34:37], v[242:245], v[170:173], v[34:37]
	s_waitcnt vmcnt(0)
	v_mfma_f32_16x16x32_bf16 v[58:61], v[246:249], v[174:177], v[58:61]
	v_mfma_f32_16x16x32_bf16 v[42:45], v[246:249], v[170:173], v[42:45]
	v_mfma_f32_16x16x32_bf16 v[30:33], v[234:237], v[166:169], v[30:33]
	v_mfma_f32_16x16x32_bf16 v[14:17], v[234:237], v[162:165], v[14:17]
	v_mfma_f32_16x16x32_bf16 v[22:25], v[238:241], v[166:169], v[22:25]
	v_mfma_f32_16x16x32_bf16 v[10:13], v[238:241], v[162:165], v[10:13]
	v_mfma_f32_16x16x32_bf16 v[18:21], v[242:245], v[166:169], v[18:21]
	v_mfma_f32_16x16x32_bf16 v[2:5], v[242:245], v[162:165], v[2:5]
	v_mfma_f32_16x16x32_bf16 v[26:29], v[246:249], v[166:169], v[26:29]
	v_mfma_f32_16x16x32_bf16 v[6:9], v[246:249], v[162:165], v[6:9]
	s_and_b64 vcc, exec, s[88:89]
	s_cbranch_vccz .LBB0_190
	s_branch .LBB0_209

; #define LOADB(dst, ks_) do { const unsigned char* ub_ = wb + (size_t)((ks_) * 144) * 1024; \
;         _Pragma("unroll") for (int j_ = 0; j_ < 8; ++j_) dst[j_] = *(const bf16x8*)(ub_ + j_ * 1024 + voff); } while (0)
; #define LOADA(fd, ks_) do { _Pragma("unroll") for (int mi_ = 0; mi_ < 4; ++mi_) fd[mi_] = AFRAG(mi_, ks_); } while (0)
; #define MMA(src, fs, ksn_) do { _Pragma("unroll") for (int mi_ = 0; mi_ < 4; ++mi_) { \
;         _Pragma("unroll") for (int j_ = 0; j_ < 8; ++j_) acc[j_][mi_] = __builtin_amdgcn_mfma_f32_16x16x32_bf16(src[j_], fs[mi_], acc[j_][mi_], 0, 0, 0); \
;         fs[mi_] = AFRAG(mi_, (ksn_) < 32 ? (ksn_) : 31); } } while (0)
; #define LOADB(dst, ks_) do { const unsigned char* ub_ = wb + (size_t)((ks_) * 64) * 1024; \
;         _Pragma("unroll") for (int j_ = 0; j_ < 8; ++j_) dst[j_] = *(const bf16x8*)(ub_ + j_ * 1024 + voff); } while (0)
; #define LOADA(fd, ks_) do { _Pragma("unroll") for (int mi_ = 0; mi_ < 4; ++mi_) fd[mi_] = AFRAG(mi_, ks_); } while (0)
; #define MMA(src, fs, ksn_) do { _Pragma("unroll") for (int mi_ = 0; mi_ < 4; ++mi_) { \
;         _Pragma("unroll") for (int j_ = 0; j_ < 8; ++j_) acc[j_][mi_] = __builtin_amdgcn_mfma_f32_16x16x32_bf16(src[j_], fs[mi_], acc[j_][mi_], 0, 0, 0); \
;         fs[mi_] = AFRAG(mi_, (ksn_) < 32 ? (ksn_) : 31); } } while (0)
; DEVINL void phase4(const Params& P, unsigned char* smem) {
;     ...
;             bf16x8 fa[4];
;             LOADB(b0, 0); LOADA(fa, 0);
; #pragma unroll 1
;             for (int ks = 0; ks < 32; ks += 2) {
;                 LOADB(b1, ks + 1);
;                 __builtin_amdgcn_sched_barrier(0);
;                 MMA(b0, fa, ks + 1);
;                 __builtin_amdgcn_sched_barrier(0);
;                 LOADB(b0, ks + 2 < 32 ? ks + 2 : 31);
;                 __builtin_amdgcn_sched_barrier(0);
;                 MMA(b1, fa, ks + 2);
;                 __builtin_amdgcn_sched_barrier(0);
;             }
.LBB0_586:
	s_add_i32 s1, s0, 2
	s_lshl_b32 s24, s1, 16
	s_add_i32 s24, s24, 0x1000
	v_xor_b32_e32 v236, v196, v238
	v_lshl_add_u32 v236, v236, 4, v191
	v_add_u32_e32 v237, 0x10000, v236
	v_lshl_add_u64 v[234:235], v[192:193], 0, s[24:25]
	s_waitcnt vmcnt(15) lgkmcnt(3)
	v_mfma_f32_16x16x32_bf16 v[126:129], v[130:133], v[174:177], v[126:129]
	s_waitcnt lgkmcnt(2)
	v_mfma_f32_16x16x32_bf16 v[122:125], v[130:133], v[170:173], v[122:125]
	s_waitcnt vmcnt(14)
	v_mfma_f32_16x16x32_bf16 v[118:121], v[134:137], v[174:177], v[118:121]
	v_mfma_f32_16x16x32_bf16 v[114:117], v[134:137], v[170:173], v[114:117]
	s_waitcnt vmcnt(13)
	v_mfma_f32_16x16x32_bf16 v[110:113], v[138:141], v[174:177], v[110:113]
	v_mfma_f32_16x16x32_bf16 v[106:109], v[138:141], v[170:173], v[106:109]
	s_waitcnt vmcnt(12)
	v_mfma_f32_16x16x32_bf16 v[102:105], v[142:145], v[174:177], v[102:105]
	v_mfma_f32_16x16x32_bf16 v[98:101], v[142:145], v[170:173], v[98:101]
	s_waitcnt lgkmcnt(1)
	v_mfma_f32_16x16x32_bf16 v[62:65], v[130:133], v[166:169], v[62:65]
	s_waitcnt lgkmcnt(0)
	v_mfma_f32_16x16x32_bf16 v[58:61], v[130:133], v[162:165], v[58:61]
	global_load_dwordx4 v[130:133], v[234:235], off offset:-4096
	v_mfma_f32_16x16x32_bf16 v[54:57], v[134:137], v[166:169], v[54:57]
	v_mfma_f32_16x16x32_bf16 v[50:53], v[134:137], v[162:165], v[50:53]
	global_load_dwordx4 v[134:137], v[234:235], off offset:-3072
	v_mfma_f32_16x16x32_bf16 v[46:49], v[138:141], v[166:169], v[46:49]
	v_mfma_f32_16x16x32_bf16 v[42:45], v[138:141], v[162:165], v[42:45]
	global_load_dwordx4 v[138:141], v[234:235], off offset:-2048
	v_mfma_f32_16x16x32_bf16 v[38:41], v[142:145], v[166:169], v[38:41]
	v_mfma_f32_16x16x32_bf16 v[34:37], v[142:145], v[162:165], v[34:37]
	global_load_dwordx4 v[142:145], v[234:235], off offset:-1024
	s_waitcnt vmcnt(15)
	v_mfma_f32_16x16x32_bf16 v[94:97], v[158:161], v[174:177], v[94:97]
	v_mfma_f32_16x16x32_bf16 v[90:93], v[158:161], v[170:173], v[90:93]
	s_waitcnt vmcnt(14)
	v_mfma_f32_16x16x32_bf16 v[86:89], v[154:157], v[174:177], v[86:89]
	v_mfma_f32_16x16x32_bf16 v[82:85], v[154:157], v[170:173], v[82:85]
	s_waitcnt vmcnt(13)
	v_mfma_f32_16x16x32_bf16 v[78:81], v[150:153], v[174:177], v[78:81]
	v_mfma_f32_16x16x32_bf16 v[74:77], v[150:153], v[170:173], v[74:77]
	s_waitcnt vmcnt(12)
	v_mfma_f32_16x16x32_bf16 v[70:73], v[146:149], v[174:177], v[70:73]
	v_mfma_f32_16x16x32_bf16 v[66:69], v[146:149], v[170:173], v[66:69]
	v_mfma_f32_16x16x32_bf16 v[30:33], v[158:161], v[166:169], v[30:33]
	v_mfma_f32_16x16x32_bf16 v[26:29], v[158:161], v[162:165], v[26:29]
	global_load_dwordx4 v[158:161], v[234:235], off
	ds_read_b128 v[174:177], v236
	v_mfma_f32_16x16x32_bf16 v[22:25], v[154:157], v[166:169], v[22:25]
	v_mfma_f32_16x16x32_bf16 v[18:21], v[154:157], v[162:165], v[18:21]
	global_load_dwordx4 v[154:157], v[234:235], off offset:1024
	ds_read_b128 v[170:173], v236 offset:32768
	v_mfma_f32_16x16x32_bf16 v[14:17], v[150:153], v[166:169], v[14:17]
	v_mfma_f32_16x16x32_bf16 v[10:13], v[150:153], v[162:165], v[10:13]
	global_load_dwordx4 v[150:153], v[234:235], off offset:2048
	v_mfma_f32_16x16x32_bf16 v[6:9], v[146:149], v[166:169], v[6:9]
	v_mfma_f32_16x16x32_bf16 v[2:5], v[146:149], v[162:165], v[2:5]
	global_load_dwordx4 v[146:149], v[234:235], off offset:3072
	ds_read_b128 v[166:169], v237
	ds_read_b128 v[162:165], v237 offset:32768
	v_lshl_add_u32 v236, s1, 2, v204
	v_lshl_add_u64 v[194:195], v[194:195], 0, s[60:61]
	v_xor_b32_e32 v236, v236, v238
	v_lshl_add_u32 v236, v236, 4, v191
	v_add_u32_e32 v237, 0x10000, v236
	s_waitcnt vmcnt(15) lgkmcnt(3)
	v_mfma_f32_16x16x32_bf16 v[126:129], v[198:201], v[174:177], v[126:129]
	s_waitcnt lgkmcnt(2)
	v_mfma_f32_16x16x32_bf16 v[122:125], v[198:201], v[170:173], v[122:125]
	s_waitcnt vmcnt(14)
	v_mfma_f32_16x16x32_bf16 v[118:121], v[206:209], v[174:177], v[118:121]
	v_mfma_f32_16x16x32_bf16 v[114:117], v[206:209], v[170:173], v[114:117]
	s_waitcnt vmcnt(13)
	v_mfma_f32_16x16x32_bf16 v[110:113], v[210:213], v[174:177], v[110:113]
	v_mfma_f32_16x16x32_bf16 v[106:109], v[210:213], v[170:173], v[106:109]
	s_waitcnt vmcnt(12)
	v_mfma_f32_16x16x32_bf16 v[102:105], v[240:243], v[174:177], v[102:105]
	v_mfma_f32_16x16x32_bf16 v[98:101], v[240:243], v[170:173], v[98:101]
	s_waitcnt lgkmcnt(1)
	v_mfma_f32_16x16x32_bf16 v[62:65], v[198:201], v[166:169], v[62:65]
	s_waitcnt lgkmcnt(0)
	v_mfma_f32_16x16x32_bf16 v[58:61], v[198:201], v[162:165], v[58:61]
	global_load_dwordx4 v[198:201], v[194:195], off offset:-4096
	v_mfma_f32_16x16x32_bf16 v[54:57], v[206:209], v[166:169], v[54:57]
	v_mfma_f32_16x16x32_bf16 v[50:53], v[206:209], v[162:165], v[50:53]
	global_load_dwordx4 v[206:209], v[194:195], off offset:-3072
	v_mfma_f32_16x16x32_bf16 v[46:49], v[210:213], v[166:169], v[46:49]
	v_mfma_f32_16x16x32_bf16 v[42:45], v[210:213], v[162:165], v[42:45]
	global_load_dwordx4 v[210:213], v[194:195], off offset:-2048
	v_mfma_f32_16x16x32_bf16 v[38:41], v[240:243], v[166:169], v[38:41]
	v_mfma_f32_16x16x32_bf16 v[34:37], v[240:243], v[162:165], v[34:37]
	global_load_dwordx4 v[240:243], v[194:195], off offset:-1024
	s_waitcnt vmcnt(15)
	v_mfma_f32_16x16x32_bf16 v[94:97], v[244:247], v[174:177], v[94:97]
	v_mfma_f32_16x16x32_bf16 v[90:93], v[244:247], v[170:173], v[90:93]
	s_waitcnt vmcnt(14)
	v_mfma_f32_16x16x32_bf16 v[86:89], v[248:251], v[174:177], v[86:89]
	v_mfma_f32_16x16x32_bf16 v[82:85], v[248:251], v[170:173], v[82:85]
	s_waitcnt vmcnt(13)
	v_mfma_f32_16x16x32_bf16 v[78:81], v[226:229], v[174:177], v[78:81]
	v_mfma_f32_16x16x32_bf16 v[74:77], v[226:229], v[170:173], v[74:77]
	s_waitcnt vmcnt(12)
	v_mfma_f32_16x16x32_bf16 v[70:73], v[230:233], v[174:177], v[70:73]
	v_mfma_f32_16x16x32_bf16 v[66:69], v[230:233], v[170:173], v[66:69]
	v_mfma_f32_16x16x32_bf16 v[30:33], v[244:247], v[166:169], v[30:33]
	v_mfma_f32_16x16x32_bf16 v[26:29], v[244:247], v[162:165], v[26:29]
	global_load_dwordx4 v[244:247], v[194:195], off
	ds_read_b128 v[174:177], v236
	v_mfma_f32_16x16x32_bf16 v[22:25], v[248:251], v[166:169], v[22:25]
	v_mfma_f32_16x16x32_bf16 v[18:21], v[248:251], v[162:165], v[18:21]
	global_load_dwordx4 v[248:251], v[194:195], off offset:1024
	ds_read_b128 v[170:173], v236 offset:32768
	v_mfma_f32_16x16x32_bf16 v[14:17], v[226:229], v[166:169], v[14:17]
	v_mfma_f32_16x16x32_bf16 v[10:13], v[226:229], v[162:165], v[10:13]
	global_load_dwordx4 v[226:229], v[194:195], off offset:2048
	v_mfma_f32_16x16x32_bf16 v[6:9], v[230:233], v[166:169], v[6:9]
	v_mfma_f32_16x16x32_bf16 v[2:5], v[230:233], v[162:165], v[2:5]
	global_load_dwordx4 v[230:233], v[194:195], off offset:3072
	ds_read_b128 v[166:169], v237
	ds_read_b128 v[162:165], v237 offset:32768
	v_add_u32_e32 v196, 8, v196
	s_mov_b32 s0, s1
	s_cmp_lt_u32 s0, 30
	s_cbranch_scc1 .LBB0_586
; #define LOADB(dst, ks_) do { const unsigned char* ub_ = wb + (size_t)((ks_) * 144) * 1024; \
;         _Pragma("unroll") for (int j_ = 0; j_ < 8; ++j_) dst[j_] = *(const bf16x8*)(ub_ + j_ * 1024 + voff); } while (0)
; #define LOADA(fd, ks_) do { _Pragma("unroll") for (int mi_ = 0; mi_ < 4; ++mi_) fd[mi_] = AFRAG(mi_, ks_); } while (0)
; #define MMA(src, fs, ksn_) do { _Pragma("unroll") for (int mi_ = 0; mi_ < 4; ++mi_) { \
;         _Pragma("unroll") for (int j_ = 0; j_ < 8; ++j_) acc[j_][mi_] = __builtin_amdgcn_mfma_f32_16x16x32_bf16(src[j_], fs[mi_], acc[j_][mi_], 0, 0, 0); \
;         fs[mi_] = AFRAG(mi_, (ksn_) < 32 ? (ksn_) : 31); } } while (0)
; #define LOADB(dst, ks_) do { const unsigned char* ub_ = wb + (size_t)((ks_) * 64) * 1024; \
;         _Pragma("unroll") for (int j_ = 0; j_ < 8; ++j_) dst[j_] = *(const bf16x8*)(ub_ + j_ * 1024 + voff); } while (0)
; #define LOADA(fd, ks_) do { _Pragma("unroll") for (int mi_ = 0; mi_ < 4; ++mi_) fd[mi_] = AFRAG(mi_, ks_); } while (0)
; #define MMA(src, fs, ksn_) do { _Pragma("unroll") for (int mi_ = 0; mi_ < 4; ++mi_) { \
;         _Pragma("unroll") for (int j_ = 0; j_ < 8; ++j_) acc[j_][mi_] = __builtin_amdgcn_mfma_f32_16x16x32_bf16(src[j_], fs[mi_], acc[j_][mi_], 0, 0, 0); \
;         fs[mi_] = AFRAG(mi_, (ksn_) < 32 ? (ksn_) : 31); } } while (0)
; DEVINL void phase4(const Params& P, unsigned char* smem) {
;     ...
;             bf16x8 fa[4];
;             LOADB(b0, 0); LOADA(fa, 0);
; #pragma unroll 1
;             for (int ks = 0; ks < 32; ks += 2) {
;                 LOADB(b1, ks + 1);
;                 __builtin_amdgcn_sched_barrier(0);
;                 MMA(b0, fa, ks + 1);
;                 __builtin_amdgcn_sched_barrier(0);
;                 LOADB(b0, ks + 2 < 32 ? ks + 2 : 31);
;                 __builtin_amdgcn_sched_barrier(0);
;                 MMA(b1, fa, ks + 2);
;                 __builtin_amdgcn_sched_barrier(0);
;             }
	v_xor_b32_e32 v236, v196, v238
	v_lshl_add_u32 v236, v236, 4, v191
	v_add_u32_e32 v237, 0x10000, v236
	s_waitcnt vmcnt(15) lgkmcnt(3)
	v_mfma_f32_16x16x32_bf16 v[126:129], v[130:133], v[174:177], v[126:129]
	s_waitcnt lgkmcnt(2)
	v_mfma_f32_16x16x32_bf16 v[122:125], v[130:133], v[170:173], v[122:125]
	s_waitcnt vmcnt(14)
	v_mfma_f32_16x16x32_bf16 v[118:121], v[134:137], v[174:177], v[118:121]
	v_mfma_f32_16x16x32_bf16 v[114:117], v[134:137], v[170:173], v[114:117]
	s_waitcnt vmcnt(13)
	v_mfma_f32_16x16x32_bf16 v[110:113], v[138:141], v[174:177], v[110:113]
	v_mfma_f32_16x16x32_bf16 v[106:109], v[138:141], v[170:173], v[106:109]
	s_waitcnt vmcnt(12)
	v_mfma_f32_16x16x32_bf16 v[102:105], v[142:145], v[174:177], v[102:105]
	v_mfma_f32_16x16x32_bf16 v[98:101], v[142:145], v[170:173], v[98:101]
	s_waitcnt lgkmcnt(1)
	v_mfma_f32_16x16x32_bf16 v[62:65], v[130:133], v[166:169], v[62:65]
	s_waitcnt lgkmcnt(0)
	v_mfma_f32_16x16x32_bf16 v[58:61], v[130:133], v[162:165], v[58:61]
	v_mfma_f32_16x16x32_bf16 v[54:57], v[134:137], v[166:169], v[54:57]
	v_mfma_f32_16x16x32_bf16 v[50:53], v[134:137], v[162:165], v[50:53]
	v_mfma_f32_16x16x32_bf16 v[46:49], v[138:141], v[166:169], v[46:49]
	v_mfma_f32_16x16x32_bf16 v[42:45], v[138:141], v[162:165], v[42:45]
	v_mfma_f32_16x16x32_bf16 v[38:41], v[142:145], v[166:169], v[38:41]
	v_mfma_f32_16x16x32_bf16 v[34:37], v[142:145], v[162:165], v[34:37]
	s_waitcnt vmcnt(11)
	v_mfma_f32_16x16x32_bf16 v[94:97], v[158:161], v[174:177], v[94:97]
	v_mfma_f32_16x16x32_bf16 v[90:93], v[158:161], v[170:173], v[90:93]
	s_waitcnt vmcnt(10)
	v_mfma_f32_16x16x32_bf16 v[86:89], v[154:157], v[174:177], v[86:89]
	v_mfma_f32_16x16x32_bf16 v[82:85], v[154:157], v[170:173], v[82:85]
	s_waitcnt vmcnt(9)
	v_mfma_f32_16x16x32_bf16 v[78:81], v[150:153], v[174:177], v[78:81]
	v_mfma_f32_16x16x32_bf16 v[74:77], v[150:153], v[170:173], v[74:77]
	s_waitcnt vmcnt(8)
	v_mfma_f32_16x16x32_bf16 v[70:73], v[146:149], v[174:177], v[70:73]
	v_mfma_f32_16x16x32_bf16 v[66:69], v[146:149], v[170:173], v[66:69]
	v_mfma_f32_16x16x32_bf16 v[30:33], v[158:161], v[166:169], v[30:33]
	v_mfma_f32_16x16x32_bf16 v[26:29], v[158:161], v[162:165], v[26:29]
	ds_read_b128 v[174:177], v236
	v_mfma_f32_16x16x32_bf16 v[22:25], v[154:157], v[166:169], v[22:25]
	v_mfma_f32_16x16x32_bf16 v[18:21], v[154:157], v[162:165], v[18:21]
	ds_read_b128 v[170:173], v236 offset:32768
	v_mfma_f32_16x16x32_bf16 v[14:17], v[150:153], v[166:169], v[14:17]
	v_mfma_f32_16x16x32_bf16 v[10:13], v[150:153], v[162:165], v[10:13]
	v_mfma_f32_16x16x32_bf16 v[6:9], v[146:149], v[166:169], v[6:9]
	v_mfma_f32_16x16x32_bf16 v[2:5], v[146:149], v[162:165], v[2:5]
	ds_read_b128 v[166:169], v237
	ds_read_b128 v[162:165], v237 offset:32768
	s_waitcnt vmcnt(7) lgkmcnt(3)
	v_mfma_f32_16x16x32_bf16 v[126:129], v[198:201], v[174:177], v[126:129]
	s_waitcnt lgkmcnt(2)
	v_mfma_f32_16x16x32_bf16 v[122:125], v[198:201], v[170:173], v[122:125]
	s_waitcnt vmcnt(6)
	v_mfma_f32_16x16x32_bf16 v[118:121], v[206:209], v[174:177], v[118:121]
	v_mfma_f32_16x16x32_bf16 v[114:117], v[206:209], v[170:173], v[114:117]
	s_waitcnt vmcnt(5)
	v_mfma_f32_16x16x32_bf16 v[110:113], v[210:213], v[174:177], v[110:113]
	v_mfma_f32_16x16x32_bf16 v[106:109], v[210:213], v[170:173], v[106:109]
	s_waitcnt vmcnt(4)
	v_mfma_f32_16x16x32_bf16 v[102:105], v[240:243], v[174:177], v[102:105]
	v_mfma_f32_16x16x32_bf16 v[98:101], v[240:243], v[170:173], v[98:101]
	s_waitcnt lgkmcnt(1)
	v_mfma_f32_16x16x32_bf16 v[62:65], v[198:201], v[166:169], v[62:65]
	s_waitcnt lgkmcnt(0)
	v_mfma_f32_16x16x32_bf16 v[58:61], v[198:201], v[162:165], v[58:61]
	v_mfma_f32_16x16x32_bf16 v[54:57], v[206:209], v[166:169], v[54:57]
	v_mfma_f32_16x16x32_bf16 v[50:53], v[206:209], v[162:165], v[50:53]
	v_mfma_f32_16x16x32_bf16 v[46:49], v[210:213], v[166:169], v[46:49]
	v_mfma_f32_16x16x32_bf16 v[42:45], v[210:213], v[162:165], v[42:45]
	v_mfma_f32_16x16x32_bf16 v[38:41], v[240:243], v[166:169], v[38:41]
	v_mfma_f32_16x16x32_bf16 v[34:37], v[240:243], v[162:165], v[34:37]
	s_waitcnt vmcnt(3)
	v_mfma_f32_16x16x32_bf16 v[94:97], v[244:247], v[174:177], v[94:97]
	v_mfma_f32_16x16x32_bf16 v[90:93], v[244:247], v[170:173], v[90:93]
	s_waitcnt vmcnt(2)
	v_mfma_f32_16x16x32_bf16 v[86:89], v[248:251], v[174:177], v[86:89]
	v_mfma_f32_16x16x32_bf16 v[82:85], v[248:251], v[170:173], v[82:85]
	s_waitcnt vmcnt(1)
	v_mfma_f32_16x16x32_bf16 v[78:81], v[226:229], v[174:177], v[78:81]
	v_mfma_f32_16x16x32_bf16 v[74:77], v[226:229], v[170:173], v[74:77]
	s_waitcnt vmcnt(0)
	v_mfma_f32_16x16x32_bf16 v[70:73], v[230:233], v[174:177], v[70:73]
	v_mfma_f32_16x16x32_bf16 v[66:69], v[230:233], v[170:173], v[66:69]
	v_mfma_f32_16x16x32_bf16 v[30:33], v[244:247], v[166:169], v[30:33]
	v_mfma_f32_16x16x32_bf16 v[26:29], v[244:247], v[162:165], v[26:29]
	v_mfma_f32_16x16x32_bf16 v[22:25], v[248:251], v[166:169], v[22:25]
	v_mfma_f32_16x16x32_bf16 v[18:21], v[248:251], v[162:165], v[18:21]
	v_mfma_f32_16x16x32_bf16 v[14:17], v[226:229], v[166:169], v[14:17]
	v_mfma_f32_16x16x32_bf16 v[10:13], v[226:229], v[162:165], v[10:13]
	v_mfma_f32_16x16x32_bf16 v[6:9], v[230:233], v[166:169], v[6:9]
	v_mfma_f32_16x16x32_bf16 v[2:5], v[230:233], v[162:165], v[2:5]
